# v71 + s_setprio 1 across the softmax VALU block of both attention loops (0 before the barrier)
# baseline (speedup 1.0000x reference)
.LBB0_1037:
	s_sub_i32 s14, s82, 63
	s_cmp_le_i32 s14, s77
	s_cselect_b64 s[4:5], -1, 0
	s_add_i32 s83, s86, 1
	s_cmp_gt_i32 s14, s77
	s_cbranch_scc1 .LBB0_1045
	s_setprio 1
	s_cmp_le_i32 s82, s0
	s_cbranch_scc1 .LBB0_1042
	v_mov_b32_e32 v90, v122
	s_nop 0
	v_cmp_gt_i32_e64 s[70:71], 26, v90
	v_cmp_gt_i32_e64 s[72:73], 27, v90
	v_cmp_gt_i32_e64 s[68:69], 25, v90
	s_and_b64 s[70:71], s[72:73], s[70:71]
	v_cmp_gt_i32_e64 s[66:67], 24, v90
	s_and_b64 s[68:69], s[70:71], s[68:69]
	v_cmp_gt_i32_e64 s[64:65], 19, v90
	s_and_b64 s[66:67], s[68:69], s[66:67]
	v_cmp_gt_i32_e64 s[62:63], 18, v90
	s_and_b64 s[64:65], s[66:67], s[64:65]
	v_cmp_gt_i32_e64 s[60:61], 17, v90
	s_and_b64 s[62:63], s[64:65], s[62:63]
	v_cmp_gt_i32_e64 s[58:59], 16, v90
	s_and_b64 s[60:61], s[62:63], s[60:61]
	v_cmp_gt_i32_e64 s[56:57], 11, v90
	s_and_b64 s[58:59], s[60:61], s[58:59]
	v_cmp_gt_i32_e64 s[54:55], 10, v90
	s_and_b64 s[56:57], s[58:59], s[56:57]
	v_cmp_gt_i32_e64 s[52:53], 9, v90
	s_and_b64 s[54:55], s[56:57], s[54:55]
	v_cmp_gt_i32_e64 s[50:51], 8, v90
	s_and_b64 s[52:53], s[54:55], s[52:53]
	v_cmp_gt_i32_e64 s[48:49], 3, v90
	s_and_b64 s[50:51], s[52:53], s[50:51]
	v_cmp_gt_i32_e64 s[46:47], 2, v90
	s_and_b64 s[48:49], s[50:51], s[48:49]
	v_cmp_gt_i32_e64 s[44:45], 1, v90
	s_and_b64 s[46:47], s[48:49], s[46:47]
	v_cmp_gt_i32_e64 s[42:43], 0, v90
	s_and_b64 s[44:45], s[46:47], s[44:45]
	s_and_b64 s[42:43], s[44:45], s[42:43]
	v_cmp_gt_i32_e64 s[40:41], 58, v90
	v_cndmask_b32_e64 v50, v50, v240, s[42:43]
	v_cmp_gt_i32_e64 s[42:43], 59, v90
	v_cmp_gt_i32_e64 s[38:39], 57, v90
	s_and_b64 s[40:41], s[42:43], s[40:41]
	v_cmp_gt_i32_e64 s[36:37], 56, v90
	s_and_b64 s[38:39], s[40:41], s[38:39]
	v_cmp_gt_i32_e64 s[34:35], 51, v90
	s_and_b64 s[36:37], s[38:39], s[36:37]
	v_cmp_gt_i32_e64 s[30:31], 50, v90
	s_and_b64 s[34:35], s[36:37], s[34:35]
	v_cmp_gt_i32_e64 s[28:29], 49, v90
	s_and_b64 s[30:31], s[34:35], s[30:31]
	v_cmp_gt_i32_e64 s[26:27], 48, v90
	s_and_b64 s[28:29], s[30:31], s[28:29]
	v_cmp_gt_i32_e64 s[24:25], 43, v90
	s_and_b64 s[26:27], s[28:29], s[26:27]
	v_cmp_gt_i32_e64 s[22:23], 42, v90
	s_and_b64 s[24:25], s[26:27], s[24:25]
	v_cmp_gt_i32_e64 s[20:21], 41, v90
	s_and_b64 s[22:23], s[24:25], s[22:23]
	v_cmp_gt_i32_e64 s[18:19], 40, v90
	s_and_b64 s[20:21], s[22:23], s[20:21]
	v_cmp_gt_i32_e64 s[16:17], 35, v90
	s_and_b64 s[18:19], s[20:21], s[18:19]
	v_cmp_gt_i32_e64 s[14:15], 34, v90
	s_and_b64 s[16:17], s[18:19], s[16:17]
	v_cmp_gt_i32_e64 s[12:13], 33, v90
	s_and_b64 s[14:15], s[16:17], s[14:15]
	v_cmp_gt_i32_e32 vcc, 32, v90
	s_and_b64 s[12:13], s[14:15], s[12:13]
	s_and_b64 vcc, s[12:13], vcc
	v_cndmask_b32_e64 v65, v65, v240, s[72:73]
	v_cndmask_b32_e64 v64, v64, v240, s[70:71]
	v_cndmask_b32_e64 v63, v63, v240, s[68:69]
	v_cndmask_b32_e64 v62, v62, v240, s[66:67]
	v_cndmask_b32_e64 v61, v61, v240, s[64:65]
	s_mov_b64 s[64:65], 0x1f040080
	v_cndmask_b32_e64 v60, v60, v240, s[62:63]
	v_cndmask_b32_e64 v59, v59, v240, s[60:61]
	v_cndmask_b32_e64 v58, v58, v240, s[58:59]
	s_mov_b64 s[58:59], 0x2000
	v_cndmask_b32_e64 v57, v57, v240, s[56:57]
	v_cndmask_b32_e64 v56, v56, v240, s[54:55]
	v_cndmask_b32_e64 v55, v55, v240, s[52:53]
	v_cndmask_b32_e64 v54, v54, v240, s[50:51]
	v_cndmask_b32_e64 v53, v53, v240, s[48:49]
	v_cndmask_b32_e64 v52, v52, v240, s[46:47]
	v_cndmask_b32_e64 v51, v51, v240, s[44:45]
	v_cndmask_b32_e64 v49, v49, v240, s[42:43]
	v_cndmask_b32_e64 v48, v48, v240, s[40:41]
	v_cndmask_b32_e64 v47, v47, v240, s[38:39]
	v_cndmask_b32_e64 v46, v46, v240, s[36:37]
	v_cndmask_b32_e64 v45, v45, v240, s[34:35]
	v_cndmask_b32_e64 v44, v44, v240, s[30:31]
	v_cndmask_b32_e64 v43, v43, v240, s[28:29]
	v_cndmask_b32_e64 v42, v42, v240, s[26:27]
	v_cndmask_b32_e64 v41, v41, v240, s[24:25]
	v_cndmask_b32_e64 v40, v40, v240, s[22:23]
	v_cndmask_b32_e64 v39, v39, v240, s[20:21]
	v_cndmask_b32_e64 v38, v38, v240, s[18:19]
	v_cndmask_b32_e64 v37, v37, v240, s[16:17]
	v_cndmask_b32_e64 v36, v36, v240, s[14:15]
	v_cndmask_b32_e64 v35, v35, v240, s[12:13]
	v_cndmask_b32_e32 v34, v34, v240, vcc

.LBB0_1066:
	v_exp_f32_e32 v50, v50
	v_exp_f32_e32 v34, v34
	v_exp_f32_e32 v51, v51
	v_exp_f32_e32 v35, v35
	v_exp_f32_e32 v52, v52
	v_exp_f32_e32 v53, v53
	v_exp_f32_e32 v36, v36
	v_exp_f32_e32 v37, v37
	v_exp_f32_e32 v54, v54
	v_exp_f32_e32 v55, v55
	v_exp_f32_e32 v38, v38
	v_exp_f32_e32 v39, v39
	v_pk_add_f32 v[92:93], v[34:35], v[50:51]
	v_exp_f32_e32 v56, v56
	v_exp_f32_e32 v57, v57
	v_pk_add_f32 v[92:93], v[52:53], v[92:93]
	v_exp_f32_e32 v40, v40
	v_exp_f32_e32 v41, v41
	v_pk_add_f32 v[92:93], v[36:37], v[92:93]
	v_exp_f32_e32 v58, v58
	v_exp_f32_e32 v59, v59
	v_pk_add_f32 v[92:93], v[54:55], v[92:93]
	v_exp_f32_e32 v42, v42
	v_exp_f32_e32 v43, v43
	v_pk_add_f32 v[92:93], v[38:39], v[92:93]
	v_exp_f32_e32 v60, v60
	v_exp_f32_e32 v61, v61
	v_pk_add_f32 v[92:93], v[56:57], v[92:93]
	v_exp_f32_e32 v44, v44
	v_exp_f32_e32 v45, v45
	v_pk_add_f32 v[92:93], v[40:41], v[92:93]
	v_exp_f32_e32 v62, v62
	v_exp_f32_e32 v63, v63
	v_pk_add_f32 v[92:93], v[58:59], v[92:93]
	v_exp_f32_e32 v46, v46
	v_exp_f32_e32 v47, v47
	v_pk_add_f32 v[92:93], v[42:43], v[92:93]
	v_exp_f32_e32 v64, v64
	v_exp_f32_e32 v65, v65
	v_pk_add_f32 v[92:93], v[60:61], v[92:93]
	v_exp_f32_e32 v48, v48
	v_exp_f32_e32 v49, v49
	v_pk_add_f32 v[92:93], v[44:45], v[92:93]
	v_cvt_pk_bf16_f32 v90, v50, v51
	v_pk_add_f32 v[92:93], v[62:63], v[92:93]
	v_cvt_pk_bf16_f32 v94, v58, v59
	v_pk_add_f32 v[92:93], v[46:47], v[92:93]
	v_cvt_pk_bf16_f32 v95, v60, v61
	v_pk_add_f32 v[92:93], v[64:65], v[92:93]
	v_cvt_pk_bf16_f32 v96, v62, v63
	v_pk_add_f32 v[92:93], v[48:49], v[92:93]
	v_cvt_pk_bf16_f32 v97, v64, v65
	v_add_f32_e32 v125, v92, v93
	v_fma_f32 v124, v124, v91, v125
	v_cvt_pk_bf16_f32 v91, v52, v53
	v_cvt_pk_bf16_f32 v92, v54, v55
	v_cvt_pk_bf16_f32 v93, v56, v57
	v_cvt_pk_bf16_f32 v98, v34, v35
	v_cvt_pk_bf16_f32 v99, v36, v37
	v_cvt_pk_bf16_f32 v100, v38, v39
	v_cvt_pk_bf16_f32 v101, v40, v41
	v_cvt_pk_bf16_f32 v102, v42, v43
	v_cvt_pk_bf16_f32 v103, v44, v45
	v_cvt_pk_bf16_f32 v104, v46, v47
	v_cvt_pk_bf16_f32 v105, v48, v49
	v_permlane32_swap_b32_e32 v90, v92
	v_permlane32_swap_b32_e32 v91, v93
	v_permlane32_swap_b32_e32 v94, v96
	v_permlane32_swap_b32_e32 v95, v97
	v_permlane32_swap_b32_e32 v98, v100
	v_permlane32_swap_b32_e32 v99, v101
	v_permlane32_swap_b32_e32 v102, v104
	v_permlane32_swap_b32_e32 v103, v105
	s_setprio 0
	s_and_b64 vcc, exec, s[6:7]
	s_mov_b64 s[12:13], -1
	s_cbranch_vccz .LBB0_1046

.LBB0_1088:
	s_add_i32 s4, s78, 1
	s_sub_i32 s14, s93, 63
	s_cmp_le_i32 s14, s80
	s_cselect_b64 s[76:77], -1, 0
	s_cmp_gt_i32 s14, s80
	s_cbranch_scc1 .LBB0_1096
	s_setprio 1
	v_cndmask_b32_e64 v0, 0, v195, s[82:83]
	v_sub_f32_e32 v0, v165, v0
	s_xor_b64 s[12:13], s[82:83], -1
	v_pk_add_f32 v[66:67], v[66:67], v[0:1] op_sel_hi:[1,0] neg_lo:[0,1] neg_hi:[0,1]
	v_pk_add_f32 v[82:83], v[82:83], v[0:1] op_sel_hi:[1,0] neg_lo:[0,1] neg_hi:[0,1]
	v_pk_add_f32 v[68:69], v[68:69], v[0:1] op_sel_hi:[1,0] neg_lo:[0,1] neg_hi:[0,1]
	v_pk_add_f32 v[84:85], v[84:85], v[0:1] op_sel_hi:[1,0] neg_lo:[0,1] neg_hi:[0,1]
	v_pk_add_f32 v[70:71], v[70:71], v[0:1] op_sel_hi:[1,0] neg_lo:[0,1] neg_hi:[0,1]
	v_pk_add_f32 v[86:87], v[86:87], v[0:1] op_sel_hi:[1,0] neg_lo:[0,1] neg_hi:[0,1]
	v_pk_add_f32 v[72:73], v[72:73], v[0:1] op_sel_hi:[1,0] neg_lo:[0,1] neg_hi:[0,1]
	v_pk_add_f32 v[88:89], v[88:89], v[0:1] op_sel_hi:[1,0] neg_lo:[0,1] neg_hi:[0,1]
	v_pk_add_f32 v[74:75], v[74:75], v[0:1] op_sel_hi:[1,0] neg_lo:[0,1] neg_hi:[0,1]
	v_pk_add_f32 v[90:91], v[90:91], v[0:1] op_sel_hi:[1,0] neg_lo:[0,1] neg_hi:[0,1]
	v_pk_add_f32 v[76:77], v[76:77], v[0:1] op_sel_hi:[1,0] neg_lo:[0,1] neg_hi:[0,1]
	v_pk_add_f32 v[92:93], v[92:93], v[0:1] op_sel_hi:[1,0] neg_lo:[0,1] neg_hi:[0,1]
	v_pk_add_f32 v[78:79], v[78:79], v[0:1] op_sel_hi:[1,0] neg_lo:[0,1] neg_hi:[0,1]
	v_pk_add_f32 v[94:95], v[94:95], v[0:1] op_sel_hi:[1,0] neg_lo:[0,1] neg_hi:[0,1]
	v_pk_add_f32 v[80:81], v[80:81], v[0:1] op_sel_hi:[1,0] neg_lo:[0,1] neg_hi:[0,1]
	s_andn2_b64 vcc, exec, s[12:13]
	v_pk_add_f32 v[96:97], v[96:97], v[0:1] op_sel_hi:[1,0] neg_lo:[0,1] neg_hi:[0,1]
	s_cbranch_vccnz .LBB0_1091
	v_mov_b32_e32 v0, v167
	ds_read_b128 v[114:117], v0
	ds_read_b128 v[118:121], v0 offset:128
	ds_read_b128 v[122:125], v0 offset:32
	ds_read_b128 v[126:129], v0 offset:160
	s_waitcnt lgkmcnt(3)
	v_sub_u32_e32 v114, v187, v114
	v_sub_u32_e32 v115, v187, v115
	s_waitcnt lgkmcnt(2)
	v_sub_u32_e32 v118, v187, v118
	v_med3_i32 v114, v114, 0, v241
	v_med3_i32 v115, v115, 0, v241
	v_sub_u32_e32 v119, v187, v119
	v_sub_u32_e32 v116, v187, v116
	v_sub_u32_e32 v120, v187, v120
	v_sub_u32_e32 v117, v187, v117
	v_sub_u32_e32 v121, v187, v121
	v_med3_i32 v118, v118, 0, v241
	v_lshl_add_u32 v114, v114, 2, s92
	v_med3_i32 v119, v119, 0, v241
	v_lshl_add_u32 v115, v115, 2, s92
	v_med3_i32 v116, v116, 0, v241
	v_med3_i32 v120, v120, 0, v241
	v_med3_i32 v117, v117, 0, v241
	v_med3_i32 v121, v121, 0, v241
	v_lshl_add_u32 v118, v118, 2, s92
	v_lshl_add_u32 v119, v119, 2, s92
	v_lshl_add_u32 v116, v116, 2, s92
	v_lshl_add_u32 v120, v120, 2, s92
	v_lshl_add_u32 v117, v117, 2, s92
	v_lshl_add_u32 v121, v121, 2, s92
	ds_read_b32 v200, v114
	ds_read_b32 v202, v118
	ds_read_b32 v201, v115
	ds_read_b32 v203, v119
	ds_read_b32 v204, v116
	ds_read_b32 v206, v120
	ds_read_b32 v205, v117
	ds_read_b32 v207, v121
	s_waitcnt lgkmcnt(9)
	v_sub_u32_e32 v114, v187, v122
	s_waitcnt lgkmcnt(8)
	v_sub_u32_e32 v115, v187, v126
	v_med3_i32 v114, v114, 0, v241
	v_med3_i32 v115, v115, 0, v241
	v_lshl_add_u32 v118, v114, 2, s92
	v_lshl_add_u32 v119, v115, 2, s92
	v_sub_u32_e32 v114, v187, v123
	v_sub_u32_e32 v115, v187, v127
	v_med3_i32 v114, v114, 0, v241
	v_med3_i32 v115, v115, 0, v241
	v_lshl_add_u32 v120, v114, 2, s92
	v_lshl_add_u32 v121, v115, 2, s92
	v_sub_u32_e32 v114, v187, v124
	v_sub_u32_e32 v115, v187, v128
	v_med3_i32 v114, v114, 0, v241
	v_med3_i32 v115, v115, 0, v241
	v_lshl_add_u32 v122, v114, 2, s92
	v_lshl_add_u32 v123, v115, 2, s92
	v_sub_u32_e32 v114, v187, v125
	v_sub_u32_e32 v115, v187, v129
	v_med3_i32 v114, v114, 0, v241
	v_med3_i32 v115, v115, 0, v241
	v_lshl_add_u32 v124, v114, 2, s92
	v_lshl_add_u32 v125, v115, 2, s92
	ds_read_b128 v[114:117], v0 offset:64
	ds_read_b32 v208, v118
	ds_read_b32 v210, v119
	ds_read_b32 v209, v120
	ds_read_b32 v211, v121
	ds_read_b32 v212, v122
	ds_read_b32 v214, v123
	ds_read_b32 v213, v124
	ds_read_b32 v215, v125
	ds_read_b128 v[118:121], v0 offset:192
	ds_read_b128 v[122:125], v0 offset:96
	s_waitcnt lgkmcnt(10)
	v_sub_u32_e32 v116, v187, v116
	v_med3_i32 v116, v116, 0, v241
	v_sub_u32_e32 v114, v187, v114
	ds_read_b128 v[126:129], v0 offset:224
	s_waitcnt lgkmcnt(2)
	v_sub_u32_e32 v0, v187, v118
	v_sub_u32_e32 v115, v187, v115
	v_sub_u32_e32 v118, v187, v119
	v_sub_u32_e32 v119, v187, v120
	v_lshl_add_u32 v120, v116, 2, s92
	v_sub_u32_e32 v116, v187, v117
	v_med3_i32 v114, v114, 0, v241
	v_med3_i32 v115, v115, 0, v241
	v_med3_i32 v118, v118, 0, v241
	v_med3_i32 v119, v119, 0, v241
	v_med3_i32 v116, v116, 0, v241
	v_sub_u32_e32 v117, v187, v121
	v_med3_i32 v0, v0, 0, v241
	v_lshl_add_u32 v114, v114, 2, s92
	v_lshl_add_u32 v115, v115, 2, s92
	v_lshl_add_u32 v118, v118, 2, s92
	v_lshl_add_u32 v119, v119, 2, s92
	v_med3_i32 v117, v117, 0, v241
	v_lshl_add_u32 v121, v116, 2, s92
	v_lshl_add_u32 v0, v0, 2, s92
	v_lshl_add_u32 v173, v117, 2, s92
	ds_read_b32 v114, v114
	ds_read_b32 v116, v0
	ds_read_b32 v115, v115
	ds_read_b32 v117, v118
	ds_read_b32 v118, v120
	ds_read_b32 v120, v119
	ds_read_b32 v119, v121
	ds_read_b32 v121, v173
	s_waitcnt lgkmcnt(9)
	v_sub_u32_e32 v0, v187, v122
	s_waitcnt lgkmcnt(8)
	v_sub_u32_e32 v122, v187, v126
	v_sub_u32_e32 v123, v187, v123
	v_sub_u32_e32 v126, v187, v127
	v_sub_u32_e32 v124, v187, v124
	v_sub_u32_e32 v127, v187, v128
	v_sub_u32_e32 v125, v187, v125
	v_sub_u32_e32 v128, v187, v129
	v_med3_i32 v0, v0, 0, v241
	v_med3_i32 v122, v122, 0, v241
	v_med3_i32 v123, v123, 0, v241
	v_med3_i32 v124, v124, 0, v241
	v_med3_i32 v125, v125, 0, v241
	v_med3_i32 v128, v128, 0, v241
	v_lshl_add_u32 v0, v0, 2, s92
	v_lshl_add_u32 v122, v122, 2, s92
	v_med3_i32 v126, v126, 0, v241
	v_lshl_add_u32 v123, v123, 2, s92
	v_med3_i32 v127, v127, 0, v241
	v_lshl_add_u32 v124, v124, 2, s92
	v_lshl_add_u32 v125, v125, 2, s92
	s_waitcnt lgkmcnt(1)
	v_pk_add_f32 v[76:77], v[76:77], v[118:119]
	v_lshl_add_u32 v119, v128, 2, s92
	v_lshl_add_u32 v126, v126, 2, s92
	v_lshl_add_u32 v127, v127, 2, s92
	v_pk_add_f32 v[74:75], v[74:75], v[114:115]
	ds_read_b32 v114, v0
	ds_read_b32 v118, v122
	ds_read_b32 v115, v123
	ds_read_b32 v122, v124
	ds_read_b32 v123, v125
	ds_read_b32 v125, v119
	ds_read_b32 v124, v127
	ds_read_b32 v119, v126
	v_pk_add_f32 v[66:67], v[66:67], v[200:201]
	v_pk_add_f32 v[68:69], v[68:69], v[204:205]
	v_pk_add_f32 v[70:71], v[70:71], v[208:209]
	v_pk_add_f32 v[72:73], v[72:73], v[212:213]
	s_waitcnt lgkmcnt(5)
	v_pk_add_f32 v[78:79], v[78:79], v[114:115]
	s_waitcnt lgkmcnt(3)
	v_pk_add_f32 v[80:81], v[80:81], v[122:123]
	v_pk_add_f32 v[82:83], v[82:83], v[202:203]
	v_pk_add_f32 v[84:85], v[84:85], v[206:207]
	v_pk_add_f32 v[86:87], v[86:87], v[210:211]
	v_pk_add_f32 v[88:89], v[88:89], v[214:215]
	v_pk_add_f32 v[90:91], v[90:91], v[116:117]
	v_pk_add_f32 v[92:93], v[92:93], v[120:121]
	s_waitcnt lgkmcnt(0)
	v_pk_add_f32 v[94:95], v[94:95], v[118:119]
	v_pk_add_f32 v[96:97], v[96:97], v[124:125]

.LBB0_1117:
	v_exp_f32_e32 v66, v66
	v_exp_f32_e32 v82, v82
	v_exp_f32_e32 v67, v67
	v_exp_f32_e32 v83, v83
	v_exp_f32_e32 v68, v68
	v_exp_f32_e32 v69, v69
	v_exp_f32_e32 v84, v84
	v_exp_f32_e32 v85, v85
	v_exp_f32_e32 v70, v70
	v_exp_f32_e32 v71, v71
	v_exp_f32_e32 v86, v86
	v_exp_f32_e32 v87, v87
	v_pk_add_f32 v[116:117], v[82:83], v[66:67]
	v_exp_f32_e32 v72, v72
	v_exp_f32_e32 v73, v73
	v_pk_add_f32 v[116:117], v[68:69], v[116:117]
	v_exp_f32_e32 v88, v88
	v_exp_f32_e32 v89, v89
	v_pk_add_f32 v[116:117], v[84:85], v[116:117]
	v_exp_f32_e32 v74, v74
	v_exp_f32_e32 v75, v75
	v_pk_add_f32 v[116:117], v[70:71], v[116:117]
	v_exp_f32_e32 v90, v90
	v_exp_f32_e32 v91, v91
	v_pk_add_f32 v[116:117], v[86:87], v[116:117]
	v_exp_f32_e32 v76, v76
	v_exp_f32_e32 v77, v77
	v_pk_add_f32 v[116:117], v[72:73], v[116:117]
	v_exp_f32_e32 v92, v92
	v_exp_f32_e32 v93, v93
	v_pk_add_f32 v[116:117], v[88:89], v[116:117]
	v_exp_f32_e32 v78, v78
	v_exp_f32_e32 v79, v79
	v_pk_add_f32 v[116:117], v[74:75], v[116:117]
	v_exp_f32_e32 v94, v94
	v_exp_f32_e32 v95, v95
	v_pk_add_f32 v[116:117], v[90:91], v[116:117]
	v_exp_f32_e32 v80, v80
	v_exp_f32_e32 v81, v81
	v_pk_add_f32 v[116:117], v[76:77], v[116:117]
	v_exp_f32_e32 v96, v96
	v_exp_f32_e32 v97, v97
	v_pk_add_f32 v[116:117], v[92:93], v[116:117]
	v_cvt_pk_bf16_f32 v115, v68, v69
	v_pk_add_f32 v[116:117], v[78:79], v[116:117]
	v_cvt_pk_bf16_f32 v118, v74, v75
	v_pk_add_f32 v[116:117], v[94:95], v[116:117]
	v_cvt_pk_bf16_f32 v119, v76, v77
	v_pk_add_f32 v[116:117], v[80:81], v[116:117]
	v_cvt_pk_bf16_f32 v120, v78, v79
	v_pk_add_f32 v[116:117], v[96:97], v[116:117]
	v_cvt_pk_bf16_f32 v121, v80, v81
	v_add_f32_e32 v0, v116, v117
	v_fma_f32 v171, v171, v114, v0
	v_cvt_pk_bf16_f32 v114, v66, v67
	v_cvt_pk_bf16_f32 v116, v70, v71
	v_cvt_pk_bf16_f32 v117, v72, v73
	v_cvt_pk_bf16_f32 v122, v82, v83
	v_cvt_pk_bf16_f32 v123, v84, v85
	v_cvt_pk_bf16_f32 v124, v86, v87
	v_cvt_pk_bf16_f32 v125, v88, v89
	v_cvt_pk_bf16_f32 v126, v90, v91
	v_cvt_pk_bf16_f32 v127, v92, v93
	v_cvt_pk_bf16_f32 v128, v94, v95
	v_cvt_pk_bf16_f32 v129, v96, v97
	v_permlane32_swap_b32_e32 v114, v116
	v_permlane32_swap_b32_e32 v115, v117
	v_permlane32_swap_b32_e32 v118, v120
	v_permlane32_swap_b32_e32 v119, v121
	v_permlane32_swap_b32_e32 v122, v124
	v_permlane32_swap_b32_e32 v123, v125
	v_permlane32_swap_b32_e32 v126, v128
	v_permlane32_swap_b32_e32 v127, v129
	s_setprio 0
	s_and_b64 vcc, exec, s[6:7]
	s_mov_b64 s[12:13], -1
	s_cbranch_vccz .LBB0_1097
